# speedup vs baseline: 1.0009x; 1.0009x over previous
.Lu0_1:
	ds_read_b64_tr_b16 v[178:179], v206 offset:24576
	ds_read_b64_tr_b16 v[180:181], v206 offset:25600
	s_waitcnt lgkmcnt(9)
	v_mfma_f32_32x32x16_f16 v[98:113], v[82:85], v[154:157], v[34:49]
	v_add_f32_e32 v86, v66, v67
	v_add_f32_e32 v86, v68, v86
	v_add_f32_e32 v86, v69, v86
	v_add_f32_e32 v86, v70, v86
	v_add_f32_e32 v86, v71, v86
	v_cvt_pk_f16_f32 v158, v66, v67
	v_cvt_pk_f16_f32 v159, v68, v69
	ds_read_b64_tr_b16 v[174:175], v207 offset:24576
	ds_read_b64_tr_b16 v[176:177], v207 offset:25600
	v_add_f32_e32 v66, v72, v86
	s_waitcnt lgkmcnt(10)
	v_mfma_f32_32x32x16_f16 v[82:97], v[170:173], v[154:157], v[34:49]
	v_add_f32_e32 v66, v73, v66
	v_add_f32_e32 v66, v74, v66
	v_add_f32_e32 v66, v75, v66
	v_cvt_pk_f16_f32 v160, v70, v71
	v_cvt_pk_f16_f32 v161, v72, v73
	ds_read_b64_tr_b16 v[170:171], v206 offset:26624
	ds_read_b64_tr_b16 v[172:173], v206 offset:27648
	s_waitcnt lgkmcnt(11)
	v_mfma_f32_32x32x16_f16 v[98:113], v[166:169], v[146:149], v[98:113]
	v_add_f32_e32 v66, v76, v66
	v_add_f32_e32 v66, v77, v66
	v_add_f32_e32 v66, v78, v66
	v_add_f32_e32 v66, v79, v66
	v_cvt_pk_f16_f32 v150, v74, v75
	v_cvt_pk_f16_f32 v151, v76, v77
	ds_read_b64_tr_b16 v[74:75], v207 offset:26624
	ds_read_b64_tr_b16 v[76:77], v207 offset:27648
	s_waitcnt lgkmcnt(12)
	v_mfma_f32_32x32x16_f16 v[82:97], v[162:165], v[146:149], v[82:97]
	v_add_f32_e32 v66, v80, v66
	v_add_f32_e32 v66, v81, v66
	v_add_f32_e32 v66, v50, v66
	v_add_f32_e32 v66, v51, v66
	v_cvt_pk_f16_f32 v152, v78, v79
	v_cvt_pk_f16_f32 v153, v80, v81
	ds_read_b64_tr_b16 v[70:71], v206 offset:28672
	ds_read_b64_tr_b16 v[72:73], v206 offset:29696
	s_waitcnt lgkmcnt(13)
	v_mfma_f32_32x32x16_f16 v[98:113], v[126:129], v[138:141], v[98:113]
	v_add_f32_e32 v66, v52, v66
	v_add_f32_e32 v66, v53, v66
	v_add_f32_e32 v66, v54, v66
	v_add_f32_e32 v78, v55, v66
	v_cvt_pk_f16_f32 v142, v50, v51
	v_cvt_pk_f16_f32 v143, v52, v53
	ds_read_b64_tr_b16 v[66:67], v207 offset:28672
	ds_read_b64_tr_b16 v[68:69], v207 offset:29696
	s_waitcnt lgkmcnt(14)
	v_mfma_f32_32x32x16_f16 v[82:97], v[122:125], v[138:141], v[82:97]
	v_add_f32_e32 v50, v56, v78
	v_add_f32_e32 v50, v57, v50
	v_add_f32_e32 v50, v58, v50
	v_add_f32_e32 v50, v59, v50
	v_cvt_pk_f16_f32 v144, v54, v55
	v_cvt_pk_f16_f32 v145, v56, v57
	ds_read_b64_tr_b16 v[54:55], v206 offset:30720
	ds_read_b64_tr_b16 v[56:57], v206 offset:31744
	s_waitcnt lgkmcnt(14)
	v_mfma_f32_32x32x16_f16 v[98:113], v[118:121], v[134:137], v[98:113]
	v_add_f32_e32 v50, v60, v50
	v_add_f32_e32 v50, v61, v50
	v_add_f32_e32 v50, v62, v50
	v_add_f32_e32 v78, v63, v50
	v_cvt_pk_f16_f32 v130, v58, v59
	v_cvt_pk_f16_f32 v131, v60, v61
	ds_read_b64_tr_b16 v[50:51], v207 offset:30720
	ds_read_b64_tr_b16 v[52:53], v207 offset:31744
	v_mfma_f32_32x32x16_f16 v[82:97], v[114:117], v[134:137], v[82:97]
	v_add_f32_e32 v58, v64, v78
	v_add_f32_e32 v60, v65, v58
	v_cvt_pk_f16_f32 v132, v62, v63
	v_cvt_pk_f16_f32 v133, v64, v65
	s_cmp_lg_u32 s47, 0
	s_cbranch_scc0 .Ldh1_skip
	s_add_i32 s26, s42, s36
	s_mov_b32 m0, s26
	s_nop 0
	global_load_lds_dwordx4 v221, s[50:51]
	s_sub_u32 s56, s50, 0x1000
	s_subb_u32 s57, s51, 0
	s_sub_i32 s26, s26, 0x1000
	s_mov_b32 m0, s26
	s_nop 0
	global_load_lds_dwordx4 v221, s[56:57]
	s_add_i32 s26, s39, s35
	s_mov_b32 m0, s26
	s_nop 0
	global_load_lds_dwordx4 v222, s[52:53]
	s_sub_u32 s56, s52, 0x1000
	s_subb_u32 s57, s53, 0
	s_sub_i32 s26, s26, 0x1000
	s_mov_b32 m0, s26
	s_nop 0
	global_load_lds_dwordx4 v222, s[56:57]

.Lu0_2:
	s_waitcnt lgkmcnt(14)
	v_mfma_f32_32x32x16_f16 v[2:17], v[158:161], v[178:181], v[2:17]
	v_exp_f32_e32 v98, v98
	v_exp_f32_e32 v99, v99
	v_exp_f32_e32 v100, v100
	v_exp_f32_e32 v101, v101
	s_waitcnt lgkmcnt(12)
	v_mfma_f32_32x32x16_f16 v[18:33], v[158:161], v[174:177], v[18:33]
	v_exp_f32_e32 v102, v102
	v_exp_f32_e32 v103, v103
	v_exp_f32_e32 v104, v104
	v_exp_f32_e32 v105, v105
	ds_read_b128 v[58:61], v211 offset:16384
	ds_read_b128 v[114:117], v211 offset:20480
	s_waitcnt lgkmcnt(12)
	v_mfma_f32_32x32x16_f16 v[2:17], v[150:153], v[170:173], v[2:17]
	v_exp_f32_e32 v106, v106
	v_exp_f32_e32 v107, v107
	v_exp_f32_e32 v108, v108
	v_exp_f32_e32 v109, v109
	ds_read_b128 v[182:185], v210 offset:16384
	ds_read_b128 v[174:177], v210 offset:20480
	s_waitcnt lgkmcnt(12)
	v_mfma_f32_32x32x16_f16 v[18:33], v[150:153], v[74:77], v[18:33]
	v_exp_f32_e32 v110, v110
	v_exp_f32_e32 v111, v111
	v_exp_f32_e32 v112, v112
	v_exp_f32_e32 v113, v113
	ds_read_b128 v[178:181], v209 offset:16384
	ds_read_b128 v[166:169], v209 offset:20480
	s_waitcnt lgkmcnt(12)
	v_mfma_f32_32x32x16_f16 v[2:17], v[142:145], v[70:73], v[2:17]
	v_exp_f32_e32 v82, v82
	v_exp_f32_e32 v83, v83
	v_exp_f32_e32 v84, v84
	v_exp_f32_e32 v85, v85
	ds_read_b128 v[170:173], v208 offset:16384
	ds_read_b128 v[162:165], v208 offset:20480
	s_waitcnt lgkmcnt(12)
	v_mfma_f32_32x32x16_f16 v[18:33], v[142:145], v[66:69], v[18:33]
	v_exp_f32_e32 v86, v86
	v_exp_f32_e32 v87, v87
	v_exp_f32_e32 v88, v88
	v_exp_f32_e32 v89, v89
	s_waitcnt lgkmcnt(10)
	v_mfma_f32_32x32x16_f16 v[2:17], v[130:133], v[54:57], v[2:17]
	v_exp_f32_e32 v90, v90
	v_exp_f32_e32 v91, v91
	v_exp_f32_e32 v92, v92
	v_exp_f32_e32 v93, v93
	s_waitcnt lgkmcnt(8)
	v_mfma_f32_32x32x16_f16 v[18:33], v[130:133], v[50:53], v[18:33]
	v_exp_f32_e32 v94, v94
	v_exp_f32_e32 v95, v95
	v_exp_f32_e32 v96, v96
	v_exp_f32_e32 v97, v97
	s_cmp_lg_u32 s47, 0
	s_cbranch_scc0 .Ldw1_o
	s_waitcnt vmcnt(4) lgkmcnt(0)
	s_branch .Ldw1_j

.Lu0_4:
	s_add_i32 s26, s39, 0x2000
	s_cmpk_lg_i32 s39, 0x4000
	s_cselect_b32 s43, s26, 0
	ds_read_b64_tr_b16 v[126:127], v206 offset:32768
	ds_read_b64_tr_b16 v[128:129], v206 offset:33792
	s_waitcnt lgkmcnt(9)
	v_mfma_f32_32x32x16_f16 v[66:81], v[58:61], v[154:157], v[34:49]
	v_add_f32_e32 v50, v98, v99
	v_add_f32_e32 v50, v100, v50
	v_add_f32_e32 v50, v101, v50
	v_add_f32_e32 v50, v102, v50
	v_add_f32_e32 v50, v103, v50
	v_cvt_pk_f16_f32 v158, v98, v99
	v_cvt_pk_f16_f32 v159, v100, v101
	ds_read_b64_tr_b16 v[122:123], v207 offset:32768
	ds_read_b64_tr_b16 v[124:125], v207 offset:33792
	v_add_f32_e32 v50, v104, v50
	v_add_f32_e32 v50, v105, v50
	v_add_f32_e32 v50, v106, v50
	v_add_f32_e32 v98, v107, v50
	s_waitcnt lgkmcnt(10)
	v_mfma_f32_32x32x16_f16 v[50:65], v[114:117], v[154:157], v[34:49]
	v_cvt_pk_f16_f32 v160, v102, v103
	v_cvt_pk_f16_f32 v161, v104, v105
	ds_read_b64_tr_b16 v[118:119], v206 offset:34816
	ds_read_b64_tr_b16 v[120:121], v206 offset:35840
	s_waitcnt lgkmcnt(11)
	v_mfma_f32_32x32x16_f16 v[66:81], v[182:185], v[146:149], v[66:81]
	v_add_f32_e32 v98, v108, v98
	v_add_f32_e32 v98, v109, v98
	v_add_f32_e32 v98, v110, v98
	v_add_f32_e32 v98, v111, v98
	v_cvt_pk_f16_f32 v150, v106, v107
	v_cvt_pk_f16_f32 v151, v108, v109
	ds_read_b64_tr_b16 v[114:115], v207 offset:34816
	ds_read_b64_tr_b16 v[116:117], v207 offset:35840
	s_waitcnt lgkmcnt(12)
	v_mfma_f32_32x32x16_f16 v[50:65], v[174:177], v[146:149], v[50:65]
	v_add_f32_e32 v98, v112, v98
	v_add_f32_e32 v98, v113, v98
	v_add_f32_e32 v98, v82, v98
	v_add_f32_e32 v98, v83, v98
	v_cvt_pk_f16_f32 v152, v110, v111
	v_cvt_pk_f16_f32 v153, v112, v113
	ds_read_b64_tr_b16 v[106:107], v206 offset:36864
	ds_read_b64_tr_b16 v[108:109], v206 offset:37888
	s_waitcnt lgkmcnt(13)
	v_mfma_f32_32x32x16_f16 v[66:81], v[178:181], v[138:141], v[66:81]
	v_add_f32_e32 v98, v84, v98
	v_add_f32_e32 v98, v85, v98
	v_add_f32_e32 v98, v86, v98
	v_add_f32_e32 v98, v87, v98
	v_cvt_pk_f16_f32 v142, v82, v83
	v_cvt_pk_f16_f32 v143, v84, v85
	ds_read_b64_tr_b16 v[102:103], v207 offset:36864
	ds_read_b64_tr_b16 v[104:105], v207 offset:37888
	s_waitcnt lgkmcnt(14)
	v_mfma_f32_32x32x16_f16 v[50:65], v[166:169], v[138:141], v[50:65]
	v_add_f32_e32 v82, v88, v98
	v_add_f32_e32 v82, v89, v82
	v_add_f32_e32 v82, v90, v82
	v_add_f32_e32 v82, v91, v82
	v_cvt_pk_f16_f32 v144, v86, v87
	v_cvt_pk_f16_f32 v145, v88, v89
	ds_read_b64_tr_b16 v[98:99], v206 offset:38912
	ds_read_b64_tr_b16 v[100:101], v206 offset:39936
	s_waitcnt lgkmcnt(14)
	v_mfma_f32_32x32x16_f16 v[66:81], v[170:173], v[134:137], v[66:81]
	v_add_f32_e32 v82, v92, v82
	v_add_f32_e32 v82, v93, v82
	v_add_f32_e32 v82, v94, v82
	v_add_f32_e32 v82, v95, v82
	v_cvt_pk_f16_f32 v130, v90, v91
	v_cvt_pk_f16_f32 v131, v92, v93
	ds_read_b64_tr_b16 v[86:87], v207 offset:38912
	ds_read_b64_tr_b16 v[88:89], v207 offset:39936
	v_mfma_f32_32x32x16_f16 v[50:65], v[162:165], v[134:137], v[50:65]
	v_add_f32_e32 v82, v96, v82
	v_add_f32_e32 v84, v97, v82
	v_cvt_pk_f16_f32 v132, v94, v95
	v_cvt_pk_f16_f32 v133, v96, v97
	s_cmp_lg_u32 s47, 0
	s_cbranch_scc0 .Ldh2_skip
	s_add_u32 s54, s50, 0x2000
	s_addc_u32 s55, s51, 0
	s_add_i32 s26, s39, s36
	s_mov_b32 m0, s26
	s_nop 0
	global_load_lds_dwordx4 v221, s[54:55]
	s_sub_u32 s56, s54, 0x1000
	s_subb_u32 s57, s55, 0
	s_sub_i32 s26, s26, 0x1000
	s_mov_b32 m0, s26
	s_nop 0
	global_load_lds_dwordx4 v221, s[56:57]
.Ldh2_join:
	v_max_f32_e32 v82, v66, v67
	s_nop 1
	v_max3_f32 v83, v68, v69, v51
	v_max3_f32 v82, v82, v50, v52
	v_max3_f32 v82, v82, v53, v70
	v_max3_f32 v83, v83, v72, v73
	v_max3_f32 v82, v82, v71, v54
	v_max3_f32 v83, v83, v56, v57
	v_max3_f32 v82, v82, v55, v74
	v_max3_f32 v83, v83, v76, v77
	v_max3_f32 v82, v82, v75, v58
	v_max3_f32 v83, v83, v60, v61
	v_max3_f32 v82, v82, v59, v78
	v_max3_f32 v83, v83, v80, v81
	v_max3_f32 v82, v82, v79, v62
	v_max3_f32 v83, v83, v64, v65
	v_max3_f32 v82, v82, v63, v83
	v_add_f32_e32 v183, v198, v84
	s_cmp_lg_u32 s47, 0
	s_cbranch_scc0 .Ldh3_skip
	s_add_u32 s54, s52, 0x2000
	s_addc_u32 s55, s53, 0
	s_add_i32 s26, s43, s35
	s_mov_b32 m0, s26
	s_nop 0
	global_load_lds_dwordx4 v222, s[54:55]
	s_sub_u32 s56, s54, 0x1000
	s_subb_u32 s57, s55, 0
	s_sub_i32 s26, s26, 0x1000
	s_mov_b32 m0, s26
	s_nop 0
	global_load_lds_dwordx4 v222, s[56:57]

.Lu0_5:
	s_waitcnt lgkmcnt(14)
	v_mfma_f32_32x32x16_f16 v[2:17], v[158:161], v[126:129], v[2:17]
	v_exp_f32_e32 v66, v66
	v_exp_f32_e32 v67, v67
	v_exp_f32_e32 v68, v68
	v_exp_f32_e32 v69, v69
	s_waitcnt lgkmcnt(12)
	v_mfma_f32_32x32x16_f16 v[18:33], v[158:161], v[122:125], v[18:33]
	v_exp_f32_e32 v70, v70
	v_exp_f32_e32 v71, v71
	v_exp_f32_e32 v72, v72
	v_exp_f32_e32 v73, v73
	ds_read_b128 v[82:85], v211
	ds_read_b128 v[170:173], v211 offset:4096
	s_waitcnt lgkmcnt(12)
	v_mfma_f32_32x32x16_f16 v[2:17], v[150:153], v[118:121], v[2:17]
	v_exp_f32_e32 v74, v74
	v_exp_f32_e32 v75, v75
	v_exp_f32_e32 v76, v76
	v_exp_f32_e32 v77, v77
	ds_read_b128 v[166:169], v210
	ds_read_b128 v[162:165], v210 offset:4096
	s_waitcnt lgkmcnt(12)
	v_mfma_f32_32x32x16_f16 v[18:33], v[150:153], v[114:117], v[18:33]
	v_exp_f32_e32 v78, v78
	v_exp_f32_e32 v79, v79
	v_exp_f32_e32 v80, v80
	v_exp_f32_e32 v81, v81
	ds_read_b128 v[126:129], v209
	ds_read_b128 v[122:125], v209 offset:4096
	s_waitcnt lgkmcnt(12)
	v_mfma_f32_32x32x16_f16 v[2:17], v[142:145], v[106:109], v[2:17]
	v_exp_f32_e32 v50, v50
	v_exp_f32_e32 v51, v51
	v_exp_f32_e32 v52, v52
	v_exp_f32_e32 v53, v53
	ds_read_b128 v[118:121], v208
	ds_read_b128 v[114:117], v208 offset:4096
	s_waitcnt lgkmcnt(12)
	v_mfma_f32_32x32x16_f16 v[18:33], v[142:145], v[102:105], v[18:33]
	v_exp_f32_e32 v54, v54
	v_exp_f32_e32 v55, v55
	v_exp_f32_e32 v56, v56
	v_exp_f32_e32 v57, v57
	s_waitcnt lgkmcnt(10)
	v_mfma_f32_32x32x16_f16 v[2:17], v[130:133], v[98:101], v[2:17]
	v_exp_f32_e32 v58, v58
	v_exp_f32_e32 v59, v59
	v_exp_f32_e32 v60, v60
	v_exp_f32_e32 v61, v61
	s_waitcnt lgkmcnt(8)
	v_mfma_f32_32x32x16_f16 v[18:33], v[130:133], v[86:89], v[18:33]
	v_exp_f32_e32 v62, v62
	v_exp_f32_e32 v63, v63
	v_exp_f32_e32 v64, v64
	v_exp_f32_e32 v65, v65
	s_cmp_lg_u32 s47, 0
	s_cbranch_scc0 .Ldw2_o
	s_waitcnt vmcnt(4) lgkmcnt(0)
	s_branch .Ldw2_j

.Lu1_1:
	ds_read_b64_tr_b16 v[178:179], v206 offset:40960
	ds_read_b64_tr_b16 v[180:181], v206 offset:41984
	s_waitcnt lgkmcnt(9)
	v_mfma_f32_32x32x16_f16 v[98:113], v[82:85], v[154:157], v[34:49]
	v_add_f32_e32 v86, v66, v67
	v_add_f32_e32 v86, v68, v86
	v_add_f32_e32 v86, v69, v86
	v_add_f32_e32 v86, v70, v86
	v_add_f32_e32 v86, v71, v86
	v_cvt_pk_f16_f32 v158, v66, v67
	v_cvt_pk_f16_f32 v159, v68, v69
	ds_read_b64_tr_b16 v[174:175], v207 offset:40960
	ds_read_b64_tr_b16 v[176:177], v207 offset:41984
	v_add_f32_e32 v66, v72, v86
	s_waitcnt lgkmcnt(10)
	v_mfma_f32_32x32x16_f16 v[82:97], v[170:173], v[154:157], v[34:49]
	v_add_f32_e32 v66, v73, v66
	v_add_f32_e32 v66, v74, v66
	v_add_f32_e32 v66, v75, v66
	v_cvt_pk_f16_f32 v160, v70, v71
	v_cvt_pk_f16_f32 v161, v72, v73
	ds_read_b64_tr_b16 v[170:171], v206 offset:43008
	ds_read_b64_tr_b16 v[172:173], v206 offset:44032
	s_waitcnt lgkmcnt(11)
	v_mfma_f32_32x32x16_f16 v[98:113], v[166:169], v[146:149], v[98:113]
	v_add_f32_e32 v66, v76, v66
	v_add_f32_e32 v66, v77, v66
	v_add_f32_e32 v66, v78, v66
	v_add_f32_e32 v66, v79, v66
	v_cvt_pk_f16_f32 v150, v74, v75
	v_cvt_pk_f16_f32 v151, v76, v77
	ds_read_b64_tr_b16 v[74:75], v207 offset:43008
	ds_read_b64_tr_b16 v[76:77], v207 offset:44032
	s_waitcnt lgkmcnt(12)
	v_mfma_f32_32x32x16_f16 v[82:97], v[162:165], v[146:149], v[82:97]
	v_add_f32_e32 v66, v80, v66
	v_add_f32_e32 v66, v81, v66
	v_add_f32_e32 v66, v50, v66
	v_add_f32_e32 v66, v51, v66
	v_cvt_pk_f16_f32 v152, v78, v79
	v_cvt_pk_f16_f32 v153, v80, v81
	ds_read_b64_tr_b16 v[70:71], v206 offset:45056
	ds_read_b64_tr_b16 v[72:73], v206 offset:46080
	s_waitcnt lgkmcnt(13)
	v_mfma_f32_32x32x16_f16 v[98:113], v[126:129], v[138:141], v[98:113]
	v_add_f32_e32 v66, v52, v66
	v_add_f32_e32 v66, v53, v66
	v_add_f32_e32 v66, v54, v66
	v_add_f32_e32 v78, v55, v66
	v_cvt_pk_f16_f32 v142, v50, v51
	v_cvt_pk_f16_f32 v143, v52, v53
	ds_read_b64_tr_b16 v[66:67], v207 offset:45056
	ds_read_b64_tr_b16 v[68:69], v207 offset:46080
	s_waitcnt lgkmcnt(14)
	v_mfma_f32_32x32x16_f16 v[82:97], v[122:125], v[138:141], v[82:97]
	v_add_f32_e32 v50, v56, v78
	v_add_f32_e32 v50, v57, v50
	v_add_f32_e32 v50, v58, v50
	v_add_f32_e32 v50, v59, v50
	v_cvt_pk_f16_f32 v144, v54, v55
	v_cvt_pk_f16_f32 v145, v56, v57
	ds_read_b64_tr_b16 v[54:55], v206 offset:47104
	ds_read_b64_tr_b16 v[56:57], v206 offset:48128
	s_waitcnt lgkmcnt(14)
	v_mfma_f32_32x32x16_f16 v[98:113], v[118:121], v[134:137], v[98:113]
	v_add_f32_e32 v50, v60, v50
	v_add_f32_e32 v50, v61, v50
	v_add_f32_e32 v50, v62, v50
	v_add_f32_e32 v78, v63, v50
	v_cvt_pk_f16_f32 v130, v58, v59
	v_cvt_pk_f16_f32 v131, v60, v61
	ds_read_b64_tr_b16 v[50:51], v207 offset:47104
	ds_read_b64_tr_b16 v[52:53], v207 offset:48128
	v_mfma_f32_32x32x16_f16 v[82:97], v[114:117], v[134:137], v[82:97]
	v_add_f32_e32 v58, v64, v78
	v_add_f32_e32 v60, v65, v58
	v_cvt_pk_f16_f32 v132, v62, v63
	v_cvt_pk_f16_f32 v133, v64, v65
	s_cmp_lg_u32 s47, 0
	s_cbranch_scc0 .Ldh4_skip
	s_add_i32 s26, s42, s36
	s_mov_b32 m0, s26
	s_nop 0
	global_load_lds_dwordx4 v221, s[50:51]
	s_sub_u32 s56, s50, 0x1000
	s_subb_u32 s57, s51, 0
	s_sub_i32 s26, s26, 0x1000
	s_mov_b32 m0, s26
	s_nop 0
	global_load_lds_dwordx4 v221, s[56:57]
	s_add_i32 s26, s39, s35
	s_mov_b32 m0, s26
	s_nop 0
	global_load_lds_dwordx4 v222, s[52:53]
	s_sub_u32 s56, s52, 0x1000
	s_subb_u32 s57, s53, 0
	s_sub_i32 s26, s26, 0x1000
	s_mov_b32 m0, s26
	s_nop 0
	global_load_lds_dwordx4 v222, s[56:57]

.Lu1_2:
	s_waitcnt lgkmcnt(14)
	v_mfma_f32_32x32x16_f16 v[2:17], v[158:161], v[178:181], v[2:17]
	v_exp_f32_e32 v98, v98
	v_exp_f32_e32 v99, v99
	v_exp_f32_e32 v100, v100
	v_exp_f32_e32 v101, v101
	s_waitcnt lgkmcnt(12)
	v_mfma_f32_32x32x16_f16 v[18:33], v[158:161], v[174:177], v[18:33]
	v_exp_f32_e32 v102, v102
	v_exp_f32_e32 v103, v103
	v_exp_f32_e32 v104, v104
	v_exp_f32_e32 v105, v105
	ds_read_b128 v[58:61], v211 offset:8192
	ds_read_b128 v[114:117], v211 offset:12288
	s_waitcnt lgkmcnt(12)
	v_mfma_f32_32x32x16_f16 v[2:17], v[150:153], v[170:173], v[2:17]
	v_exp_f32_e32 v106, v106
	v_exp_f32_e32 v107, v107
	v_exp_f32_e32 v108, v108
	v_exp_f32_e32 v109, v109
	ds_read_b128 v[182:185], v210 offset:8192
	ds_read_b128 v[174:177], v210 offset:12288
	s_waitcnt lgkmcnt(12)
	v_mfma_f32_32x32x16_f16 v[18:33], v[150:153], v[74:77], v[18:33]
	v_exp_f32_e32 v110, v110
	v_exp_f32_e32 v111, v111
	v_exp_f32_e32 v112, v112
	v_exp_f32_e32 v113, v113
	ds_read_b128 v[178:181], v209 offset:8192
	ds_read_b128 v[166:169], v209 offset:12288
	s_waitcnt lgkmcnt(12)
	v_mfma_f32_32x32x16_f16 v[2:17], v[142:145], v[70:73], v[2:17]
	v_exp_f32_e32 v82, v82
	v_exp_f32_e32 v83, v83
	v_exp_f32_e32 v84, v84
	v_exp_f32_e32 v85, v85
	ds_read_b128 v[170:173], v208 offset:8192
	ds_read_b128 v[162:165], v208 offset:12288
	s_waitcnt lgkmcnt(12)
	v_mfma_f32_32x32x16_f16 v[18:33], v[142:145], v[66:69], v[18:33]
	v_exp_f32_e32 v86, v86
	v_exp_f32_e32 v87, v87
	v_exp_f32_e32 v88, v88
	v_exp_f32_e32 v89, v89
	s_waitcnt lgkmcnt(10)
	v_mfma_f32_32x32x16_f16 v[2:17], v[130:133], v[54:57], v[2:17]
	v_exp_f32_e32 v90, v90
	v_exp_f32_e32 v91, v91
	v_exp_f32_e32 v92, v92
	v_exp_f32_e32 v93, v93
	s_waitcnt lgkmcnt(8)
	v_mfma_f32_32x32x16_f16 v[18:33], v[130:133], v[50:53], v[18:33]
	v_exp_f32_e32 v94, v94
	v_exp_f32_e32 v95, v95
	v_exp_f32_e32 v96, v96
	v_exp_f32_e32 v97, v97
	s_cmp_lg_u32 s47, 0
	s_cbranch_scc0 .Ldw3_o
	s_waitcnt vmcnt(4) lgkmcnt(0)
	s_branch .Ldw3_j

.Lu1_4:
	s_add_i32 s26, s39, 0x2000
	s_cmpk_lg_i32 s39, 0x4000
	s_cselect_b32 s43, s26, 0
	ds_read_b64_tr_b16 v[126:127], v206 offset:24576
	ds_read_b64_tr_b16 v[128:129], v206 offset:25600
	s_waitcnt lgkmcnt(9)
	v_mfma_f32_32x32x16_f16 v[66:81], v[58:61], v[154:157], v[34:49]
	v_add_f32_e32 v50, v98, v99
	v_add_f32_e32 v50, v100, v50
	v_add_f32_e32 v50, v101, v50
	v_add_f32_e32 v50, v102, v50
	v_add_f32_e32 v50, v103, v50
	v_cvt_pk_f16_f32 v158, v98, v99
	v_cvt_pk_f16_f32 v159, v100, v101
	ds_read_b64_tr_b16 v[122:123], v207 offset:24576
	ds_read_b64_tr_b16 v[124:125], v207 offset:25600
	v_add_f32_e32 v50, v104, v50
	v_add_f32_e32 v50, v105, v50
	v_add_f32_e32 v50, v106, v50
	v_add_f32_e32 v98, v107, v50
	s_waitcnt lgkmcnt(10)
	v_mfma_f32_32x32x16_f16 v[50:65], v[114:117], v[154:157], v[34:49]
	v_cvt_pk_f16_f32 v160, v102, v103
	v_cvt_pk_f16_f32 v161, v104, v105
	ds_read_b64_tr_b16 v[118:119], v206 offset:26624
	ds_read_b64_tr_b16 v[120:121], v206 offset:27648
	s_waitcnt lgkmcnt(11)
	v_mfma_f32_32x32x16_f16 v[66:81], v[182:185], v[146:149], v[66:81]
	v_add_f32_e32 v98, v108, v98
	v_add_f32_e32 v98, v109, v98
	v_add_f32_e32 v98, v110, v98
	v_add_f32_e32 v98, v111, v98
	v_cvt_pk_f16_f32 v150, v106, v107
	v_cvt_pk_f16_f32 v151, v108, v109
	ds_read_b64_tr_b16 v[114:115], v207 offset:26624
	ds_read_b64_tr_b16 v[116:117], v207 offset:27648
	s_waitcnt lgkmcnt(12)
	v_mfma_f32_32x32x16_f16 v[50:65], v[174:177], v[146:149], v[50:65]
	v_add_f32_e32 v98, v112, v98
	v_add_f32_e32 v98, v113, v98
	v_add_f32_e32 v98, v82, v98
	v_add_f32_e32 v98, v83, v98
	v_cvt_pk_f16_f32 v152, v110, v111
	v_cvt_pk_f16_f32 v153, v112, v113
	ds_read_b64_tr_b16 v[106:107], v206 offset:28672
	ds_read_b64_tr_b16 v[108:109], v206 offset:29696
	s_waitcnt lgkmcnt(13)
	v_mfma_f32_32x32x16_f16 v[66:81], v[178:181], v[138:141], v[66:81]
	v_add_f32_e32 v98, v84, v98
	v_add_f32_e32 v98, v85, v98
	v_add_f32_e32 v98, v86, v98
	v_add_f32_e32 v98, v87, v98
	v_cvt_pk_f16_f32 v142, v82, v83
	v_cvt_pk_f16_f32 v143, v84, v85
	ds_read_b64_tr_b16 v[102:103], v207 offset:28672
	ds_read_b64_tr_b16 v[104:105], v207 offset:29696
	s_waitcnt lgkmcnt(14)
	v_mfma_f32_32x32x16_f16 v[50:65], v[166:169], v[138:141], v[50:65]
	v_add_f32_e32 v82, v88, v98
	v_add_f32_e32 v82, v89, v82
	v_add_f32_e32 v82, v90, v82
	v_add_f32_e32 v82, v91, v82
	v_cvt_pk_f16_f32 v144, v86, v87
	v_cvt_pk_f16_f32 v145, v88, v89
	ds_read_b64_tr_b16 v[98:99], v206 offset:30720
	ds_read_b64_tr_b16 v[100:101], v206 offset:31744
	s_waitcnt lgkmcnt(14)
	v_mfma_f32_32x32x16_f16 v[66:81], v[170:173], v[134:137], v[66:81]
	v_add_f32_e32 v82, v92, v82
	v_add_f32_e32 v82, v93, v82
	v_add_f32_e32 v82, v94, v82
	v_add_f32_e32 v82, v95, v82
	v_cvt_pk_f16_f32 v130, v90, v91
	v_cvt_pk_f16_f32 v131, v92, v93
	ds_read_b64_tr_b16 v[86:87], v207 offset:30720
	ds_read_b64_tr_b16 v[88:89], v207 offset:31744
	v_mfma_f32_32x32x16_f16 v[50:65], v[162:165], v[134:137], v[50:65]
	v_add_f32_e32 v82, v96, v82
	v_add_f32_e32 v84, v97, v82
	v_cvt_pk_f16_f32 v132, v94, v95
	v_cvt_pk_f16_f32 v133, v96, v97
	s_cmp_lg_u32 s47, 0
	s_cbranch_scc0 .Ldh5_skip
	s_add_u32 s54, s50, 0x2000
	s_addc_u32 s55, s51, 0
	s_add_i32 s26, s39, s36
	s_mov_b32 m0, s26
	s_nop 0
	global_load_lds_dwordx4 v221, s[54:55]
	s_sub_u32 s56, s54, 0x1000
	s_subb_u32 s57, s55, 0
	s_sub_i32 s26, s26, 0x1000
	s_mov_b32 m0, s26
	s_nop 0
	global_load_lds_dwordx4 v221, s[56:57]

.Lu1_5:
	s_waitcnt lgkmcnt(14)
	v_mfma_f32_32x32x16_f16 v[2:17], v[158:161], v[126:129], v[2:17]
	v_exp_f32_e32 v66, v66
	v_exp_f32_e32 v67, v67
	v_exp_f32_e32 v68, v68
	v_exp_f32_e32 v69, v69
	s_waitcnt lgkmcnt(12)
	v_mfma_f32_32x32x16_f16 v[18:33], v[158:161], v[122:125], v[18:33]
	v_exp_f32_e32 v70, v70
	v_exp_f32_e32 v71, v71
	v_exp_f32_e32 v72, v72
	v_exp_f32_e32 v73, v73
	ds_read_b128 v[82:85], v211 offset:16384
	ds_read_b128 v[170:173], v211 offset:20480
	s_waitcnt lgkmcnt(12)
	v_mfma_f32_32x32x16_f16 v[2:17], v[150:153], v[118:121], v[2:17]
	v_exp_f32_e32 v74, v74
	v_exp_f32_e32 v75, v75
	v_exp_f32_e32 v76, v76
	v_exp_f32_e32 v77, v77
	ds_read_b128 v[166:169], v210 offset:16384
	ds_read_b128 v[162:165], v210 offset:20480
	s_waitcnt lgkmcnt(12)
	v_mfma_f32_32x32x16_f16 v[18:33], v[150:153], v[114:117], v[18:33]
	v_exp_f32_e32 v78, v78
	v_exp_f32_e32 v79, v79
	v_exp_f32_e32 v80, v80
	v_exp_f32_e32 v81, v81
	ds_read_b128 v[126:129], v209 offset:16384
	ds_read_b128 v[122:125], v209 offset:20480
	s_waitcnt lgkmcnt(12)
	v_mfma_f32_32x32x16_f16 v[2:17], v[142:145], v[106:109], v[2:17]
	v_exp_f32_e32 v50, v50
	v_exp_f32_e32 v51, v51
	v_exp_f32_e32 v52, v52
	v_exp_f32_e32 v53, v53
	ds_read_b128 v[118:121], v208 offset:16384
	ds_read_b128 v[114:117], v208 offset:20480
	s_waitcnt lgkmcnt(12)
	v_mfma_f32_32x32x16_f16 v[18:33], v[142:145], v[102:105], v[18:33]
	v_exp_f32_e32 v54, v54
	v_exp_f32_e32 v55, v55
	v_exp_f32_e32 v56, v56
	v_exp_f32_e32 v57, v57
	s_waitcnt lgkmcnt(10)
	v_mfma_f32_32x32x16_f16 v[2:17], v[130:133], v[98:101], v[2:17]
	v_exp_f32_e32 v58, v58
	v_exp_f32_e32 v59, v59
	v_exp_f32_e32 v60, v60
	v_exp_f32_e32 v61, v61
	s_waitcnt lgkmcnt(8)
	v_mfma_f32_32x32x16_f16 v[18:33], v[130:133], v[86:89], v[18:33]
	v_exp_f32_e32 v62, v62
	v_exp_f32_e32 v63, v63
	v_exp_f32_e32 v64, v64
	v_exp_f32_e32 v65, v65
	s_cmp_lg_u32 s47, 0
	s_cbranch_scc0 .Ldw4_o
	s_waitcnt vmcnt(4) lgkmcnt(0)
	s_branch .Ldw4_j

.Lu2_1:
	ds_read_b64_tr_b16 v[178:179], v206 offset:32768
	ds_read_b64_tr_b16 v[180:181], v206 offset:33792
	s_waitcnt lgkmcnt(9)
	v_mfma_f32_32x32x16_f16 v[98:113], v[82:85], v[154:157], v[34:49]
	v_add_f32_e32 v86, v66, v67
	v_add_f32_e32 v86, v68, v86
	v_add_f32_e32 v86, v69, v86
	v_add_f32_e32 v86, v70, v86
	v_add_f32_e32 v86, v71, v86
	v_cvt_pk_f16_f32 v158, v66, v67
	v_cvt_pk_f16_f32 v159, v68, v69
	ds_read_b64_tr_b16 v[174:175], v207 offset:32768
	ds_read_b64_tr_b16 v[176:177], v207 offset:33792
	v_add_f32_e32 v66, v72, v86
	s_waitcnt lgkmcnt(10)
	v_mfma_f32_32x32x16_f16 v[82:97], v[170:173], v[154:157], v[34:49]
	v_add_f32_e32 v66, v73, v66
	v_add_f32_e32 v66, v74, v66
	v_add_f32_e32 v66, v75, v66
	v_cvt_pk_f16_f32 v160, v70, v71
	v_cvt_pk_f16_f32 v161, v72, v73
	ds_read_b64_tr_b16 v[170:171], v206 offset:34816
	ds_read_b64_tr_b16 v[172:173], v206 offset:35840
	s_waitcnt lgkmcnt(11)
	v_mfma_f32_32x32x16_f16 v[98:113], v[166:169], v[146:149], v[98:113]
	v_add_f32_e32 v66, v76, v66
	v_add_f32_e32 v66, v77, v66
	v_add_f32_e32 v66, v78, v66
	v_add_f32_e32 v66, v79, v66
	v_cvt_pk_f16_f32 v150, v74, v75
	v_cvt_pk_f16_f32 v151, v76, v77
	ds_read_b64_tr_b16 v[74:75], v207 offset:34816
	ds_read_b64_tr_b16 v[76:77], v207 offset:35840
	s_waitcnt lgkmcnt(12)
	v_mfma_f32_32x32x16_f16 v[82:97], v[162:165], v[146:149], v[82:97]
	v_add_f32_e32 v66, v80, v66
	v_add_f32_e32 v66, v81, v66
	v_add_f32_e32 v66, v50, v66
	v_add_f32_e32 v66, v51, v66
	v_cvt_pk_f16_f32 v152, v78, v79
	v_cvt_pk_f16_f32 v153, v80, v81
	ds_read_b64_tr_b16 v[70:71], v206 offset:36864
	ds_read_b64_tr_b16 v[72:73], v206 offset:37888
	s_waitcnt lgkmcnt(13)
	v_mfma_f32_32x32x16_f16 v[98:113], v[126:129], v[138:141], v[98:113]
	v_add_f32_e32 v66, v52, v66
	v_add_f32_e32 v66, v53, v66
	v_add_f32_e32 v66, v54, v66
	v_add_f32_e32 v78, v55, v66
	v_cvt_pk_f16_f32 v142, v50, v51
	v_cvt_pk_f16_f32 v143, v52, v53
	ds_read_b64_tr_b16 v[66:67], v207 offset:36864
	ds_read_b64_tr_b16 v[68:69], v207 offset:37888
	s_waitcnt lgkmcnt(14)
	v_mfma_f32_32x32x16_f16 v[82:97], v[122:125], v[138:141], v[82:97]
	v_add_f32_e32 v50, v56, v78
	v_add_f32_e32 v50, v57, v50
	v_add_f32_e32 v50, v58, v50
	v_add_f32_e32 v50, v59, v50
	v_cvt_pk_f16_f32 v144, v54, v55
	v_cvt_pk_f16_f32 v145, v56, v57
	ds_read_b64_tr_b16 v[54:55], v206 offset:38912
	ds_read_b64_tr_b16 v[56:57], v206 offset:39936
	s_waitcnt lgkmcnt(14)
	v_mfma_f32_32x32x16_f16 v[98:113], v[118:121], v[134:137], v[98:113]
	v_add_f32_e32 v50, v60, v50
	v_add_f32_e32 v50, v61, v50
	v_add_f32_e32 v50, v62, v50
	v_add_f32_e32 v78, v63, v50
	v_cvt_pk_f16_f32 v130, v58, v59
	v_cvt_pk_f16_f32 v131, v60, v61
	ds_read_b64_tr_b16 v[50:51], v207 offset:38912
	ds_read_b64_tr_b16 v[52:53], v207 offset:39936
	v_mfma_f32_32x32x16_f16 v[82:97], v[114:117], v[134:137], v[82:97]
	v_add_f32_e32 v58, v64, v78
	v_add_f32_e32 v60, v65, v58
	v_cvt_pk_f16_f32 v132, v62, v63
	v_cvt_pk_f16_f32 v133, v64, v65
	s_cmp_lg_u32 s47, 0
	s_cbranch_scc0 .Ldh7_skip
	s_add_i32 s26, s42, s36
	s_mov_b32 m0, s26
	s_nop 0
	global_load_lds_dwordx4 v221, s[50:51]
	s_sub_u32 s56, s50, 0x1000
	s_subb_u32 s57, s51, 0
	s_sub_i32 s26, s26, 0x1000
	s_mov_b32 m0, s26
	s_nop 0
	global_load_lds_dwordx4 v221, s[56:57]
	s_add_i32 s26, s39, s35
	s_mov_b32 m0, s26
	s_nop 0
	global_load_lds_dwordx4 v222, s[52:53]
	s_sub_u32 s56, s52, 0x1000
	s_subb_u32 s57, s53, 0
	s_sub_i32 s26, s26, 0x1000
	s_mov_b32 m0, s26
	s_nop 0
	global_load_lds_dwordx4 v222, s[56:57]

.Lu2_2:
	s_waitcnt lgkmcnt(14)
	v_mfma_f32_32x32x16_f16 v[2:17], v[158:161], v[178:181], v[2:17]
	v_exp_f32_e32 v98, v98
	v_exp_f32_e32 v99, v99
	v_exp_f32_e32 v100, v100
	v_exp_f32_e32 v101, v101
	s_waitcnt lgkmcnt(12)
	v_mfma_f32_32x32x16_f16 v[18:33], v[158:161], v[174:177], v[18:33]
	v_exp_f32_e32 v102, v102
	v_exp_f32_e32 v103, v103
	v_exp_f32_e32 v104, v104
	v_exp_f32_e32 v105, v105
	ds_read_b128 v[58:61], v211
	ds_read_b128 v[114:117], v211 offset:4096
	s_waitcnt lgkmcnt(12)
	v_mfma_f32_32x32x16_f16 v[2:17], v[150:153], v[170:173], v[2:17]
	v_exp_f32_e32 v106, v106
	v_exp_f32_e32 v107, v107
	v_exp_f32_e32 v108, v108
	v_exp_f32_e32 v109, v109
	ds_read_b128 v[182:185], v210
	ds_read_b128 v[174:177], v210 offset:4096
	s_waitcnt lgkmcnt(12)
	v_mfma_f32_32x32x16_f16 v[18:33], v[150:153], v[74:77], v[18:33]
	v_exp_f32_e32 v110, v110
	v_exp_f32_e32 v111, v111
	v_exp_f32_e32 v112, v112
	v_exp_f32_e32 v113, v113
	ds_read_b128 v[178:181], v209
	ds_read_b128 v[166:169], v209 offset:4096
	s_waitcnt lgkmcnt(12)
	v_mfma_f32_32x32x16_f16 v[2:17], v[142:145], v[70:73], v[2:17]
	v_exp_f32_e32 v82, v82
	v_exp_f32_e32 v83, v83
	v_exp_f32_e32 v84, v84
	v_exp_f32_e32 v85, v85
	ds_read_b128 v[170:173], v208
	ds_read_b128 v[162:165], v208 offset:4096
	s_waitcnt lgkmcnt(12)
	v_mfma_f32_32x32x16_f16 v[18:33], v[142:145], v[66:69], v[18:33]
	v_exp_f32_e32 v86, v86
	v_exp_f32_e32 v87, v87
	v_exp_f32_e32 v88, v88
	v_exp_f32_e32 v89, v89
	s_waitcnt lgkmcnt(10)
	v_mfma_f32_32x32x16_f16 v[2:17], v[130:133], v[54:57], v[2:17]
	v_exp_f32_e32 v90, v90
	v_exp_f32_e32 v91, v91
	v_exp_f32_e32 v92, v92
	v_exp_f32_e32 v93, v93
	s_waitcnt lgkmcnt(8)
	v_mfma_f32_32x32x16_f16 v[18:33], v[130:133], v[50:53], v[18:33]
	v_exp_f32_e32 v94, v94
	v_exp_f32_e32 v95, v95
	v_exp_f32_e32 v96, v96
	v_exp_f32_e32 v97, v97
	s_cmp_lg_u32 s47, 0
	s_cbranch_scc0 .Ldw5_o
	s_waitcnt vmcnt(4) lgkmcnt(0)
	s_branch .Ldw5_j

.Lu2_4:
	s_add_i32 s26, s39, 0x2000
	s_cmpk_lg_i32 s39, 0x4000
	s_cselect_b32 s43, s26, 0
	ds_read_b64_tr_b16 v[126:127], v206 offset:40960
	ds_read_b64_tr_b16 v[128:129], v206 offset:41984
	s_waitcnt lgkmcnt(9)
	v_mfma_f32_32x32x16_f16 v[66:81], v[58:61], v[154:157], v[34:49]
	v_add_f32_e32 v50, v98, v99
	v_add_f32_e32 v50, v100, v50
	v_add_f32_e32 v50, v101, v50
	v_add_f32_e32 v50, v102, v50
	v_add_f32_e32 v50, v103, v50
	v_cvt_pk_f16_f32 v158, v98, v99
	v_cvt_pk_f16_f32 v159, v100, v101
	ds_read_b64_tr_b16 v[122:123], v207 offset:40960
	ds_read_b64_tr_b16 v[124:125], v207 offset:41984
	v_add_f32_e32 v50, v104, v50
	v_add_f32_e32 v50, v105, v50
	v_add_f32_e32 v50, v106, v50
	v_add_f32_e32 v98, v107, v50
	s_waitcnt lgkmcnt(10)
	v_mfma_f32_32x32x16_f16 v[50:65], v[114:117], v[154:157], v[34:49]
	v_cvt_pk_f16_f32 v160, v102, v103
	v_cvt_pk_f16_f32 v161, v104, v105
	ds_read_b64_tr_b16 v[118:119], v206 offset:43008
	ds_read_b64_tr_b16 v[120:121], v206 offset:44032
	s_waitcnt lgkmcnt(11)
	v_mfma_f32_32x32x16_f16 v[66:81], v[182:185], v[146:149], v[66:81]
	v_add_f32_e32 v98, v108, v98
	v_add_f32_e32 v98, v109, v98
	v_add_f32_e32 v98, v110, v98
	v_add_f32_e32 v98, v111, v98
	v_cvt_pk_f16_f32 v150, v106, v107
	v_cvt_pk_f16_f32 v151, v108, v109
	ds_read_b64_tr_b16 v[114:115], v207 offset:43008
	ds_read_b64_tr_b16 v[116:117], v207 offset:44032
	s_waitcnt lgkmcnt(12)
	v_mfma_f32_32x32x16_f16 v[50:65], v[174:177], v[146:149], v[50:65]
	v_add_f32_e32 v98, v112, v98
	v_add_f32_e32 v98, v113, v98
	v_add_f32_e32 v98, v82, v98
	v_add_f32_e32 v98, v83, v98
	v_cvt_pk_f16_f32 v152, v110, v111
	v_cvt_pk_f16_f32 v153, v112, v113
	ds_read_b64_tr_b16 v[106:107], v206 offset:45056
	ds_read_b64_tr_b16 v[108:109], v206 offset:46080
	s_waitcnt lgkmcnt(13)
	v_mfma_f32_32x32x16_f16 v[66:81], v[178:181], v[138:141], v[66:81]
	v_add_f32_e32 v98, v84, v98
	v_add_f32_e32 v98, v85, v98
	v_add_f32_e32 v98, v86, v98
	v_add_f32_e32 v98, v87, v98
	v_cvt_pk_f16_f32 v142, v82, v83
	v_cvt_pk_f16_f32 v143, v84, v85
	ds_read_b64_tr_b16 v[102:103], v207 offset:45056
	ds_read_b64_tr_b16 v[104:105], v207 offset:46080
	s_waitcnt lgkmcnt(14)
	v_mfma_f32_32x32x16_f16 v[50:65], v[166:169], v[138:141], v[50:65]
	v_add_f32_e32 v82, v88, v98
	v_add_f32_e32 v82, v89, v82
	v_add_f32_e32 v82, v90, v82
	v_add_f32_e32 v82, v91, v82
	v_cvt_pk_f16_f32 v144, v86, v87
	v_cvt_pk_f16_f32 v145, v88, v89
	ds_read_b64_tr_b16 v[98:99], v206 offset:47104
	ds_read_b64_tr_b16 v[100:101], v206 offset:48128
	s_waitcnt lgkmcnt(14)
	v_mfma_f32_32x32x16_f16 v[66:81], v[170:173], v[134:137], v[66:81]
	v_add_f32_e32 v82, v92, v82
	v_add_f32_e32 v82, v93, v82
	v_add_f32_e32 v82, v94, v82
	v_add_f32_e32 v82, v95, v82
	v_cvt_pk_f16_f32 v130, v90, v91
	v_cvt_pk_f16_f32 v131, v92, v93
	ds_read_b64_tr_b16 v[86:87], v207 offset:47104
	ds_read_b64_tr_b16 v[88:89], v207 offset:48128
	v_mfma_f32_32x32x16_f16 v[50:65], v[162:165], v[134:137], v[50:65]
	v_add_f32_e32 v82, v96, v82
	v_add_f32_e32 v84, v97, v82
	v_cvt_pk_f16_f32 v132, v94, v95
	v_cvt_pk_f16_f32 v133, v96, v97
	s_cmp_lg_u32 s47, 0
	s_cbranch_scc0 .Ldh8_skip
	s_add_u32 s54, s50, 0x2000
	s_addc_u32 s55, s51, 0
	s_add_i32 s26, s39, s36
	s_mov_b32 m0, s26
	s_nop 0
	global_load_lds_dwordx4 v221, s[54:55]
	s_sub_u32 s56, s54, 0x1000
	s_subb_u32 s57, s55, 0
	s_sub_i32 s26, s26, 0x1000
	s_mov_b32 m0, s26
	s_nop 0
	global_load_lds_dwordx4 v221, s[56:57]

.Lu2_5:
	s_waitcnt lgkmcnt(14)
	v_mfma_f32_32x32x16_f16 v[2:17], v[158:161], v[126:129], v[2:17]
	v_exp_f32_e32 v66, v66
	v_exp_f32_e32 v67, v67
	v_exp_f32_e32 v68, v68
	v_exp_f32_e32 v69, v69
	s_waitcnt lgkmcnt(12)
	v_mfma_f32_32x32x16_f16 v[18:33], v[158:161], v[122:125], v[18:33]
	v_exp_f32_e32 v70, v70
	v_exp_f32_e32 v71, v71
	v_exp_f32_e32 v72, v72
	v_exp_f32_e32 v73, v73
	ds_read_b128 v[82:85], v211 offset:8192
	ds_read_b128 v[170:173], v211 offset:12288
	s_waitcnt lgkmcnt(12)
	v_mfma_f32_32x32x16_f16 v[2:17], v[150:153], v[118:121], v[2:17]
	v_exp_f32_e32 v74, v74
	v_exp_f32_e32 v75, v75
	v_exp_f32_e32 v76, v76
	v_exp_f32_e32 v77, v77
	ds_read_b128 v[166:169], v210 offset:8192
	ds_read_b128 v[162:165], v210 offset:12288
	s_waitcnt lgkmcnt(12)
	v_mfma_f32_32x32x16_f16 v[18:33], v[150:153], v[114:117], v[18:33]
	v_exp_f32_e32 v78, v78
	v_exp_f32_e32 v79, v79
	v_exp_f32_e32 v80, v80
	v_exp_f32_e32 v81, v81
	ds_read_b128 v[126:129], v209 offset:8192
	ds_read_b128 v[122:125], v209 offset:12288
	s_waitcnt lgkmcnt(12)
	v_mfma_f32_32x32x16_f16 v[2:17], v[142:145], v[106:109], v[2:17]
	v_exp_f32_e32 v50, v50
	v_exp_f32_e32 v51, v51
	v_exp_f32_e32 v52, v52
	v_exp_f32_e32 v53, v53
	ds_read_b128 v[118:121], v208 offset:8192
	ds_read_b128 v[114:117], v208 offset:12288
	s_waitcnt lgkmcnt(12)
	v_mfma_f32_32x32x16_f16 v[18:33], v[142:145], v[102:105], v[18:33]
	v_exp_f32_e32 v54, v54
	v_exp_f32_e32 v55, v55
	v_exp_f32_e32 v56, v56
	v_exp_f32_e32 v57, v57
	s_waitcnt lgkmcnt(10)
	v_mfma_f32_32x32x16_f16 v[2:17], v[130:133], v[98:101], v[2:17]
	v_exp_f32_e32 v58, v58
	v_exp_f32_e32 v59, v59
	v_exp_f32_e32 v60, v60
	v_exp_f32_e32 v61, v61
	s_waitcnt lgkmcnt(8)
	v_mfma_f32_32x32x16_f16 v[18:33], v[130:133], v[86:89], v[18:33]
	v_exp_f32_e32 v62, v62
	v_exp_f32_e32 v63, v63
	v_exp_f32_e32 v64, v64
	v_exp_f32_e32 v65, v65
	s_cmp_lg_u32 s47, 0
	s_cbranch_scc0 .Ldw6_o
	s_waitcnt vmcnt(4) lgkmcnt(0)
	s_branch .Ldw6_j
